# static s_setprio 1 for waves 4-7 (younger half) at the start of the stick-breaking attention items
# speedup vs baseline: 1.0038x; 1.0035x over previous
.LBB0_586:
	s_and_b64 vcc, exec, s[10:11]
	s_cbranch_vccz .LBB0_496
	s_and_b64 vcc, exec, s[82:83]
	s_cbranch_vccnz .Lprio_skip_0
	s_setprio 1
.Lprio_skip_0:
	s_sub_i32 s55, 63, s59
	s_load_dwordx2 s[10:11], s[76:77], 0x108
	s_load_dwordx2 s[92:93], s[76:77], 0x130
	v_mov_b32_e32 v48, v108
	s_lshl_b32 s62, s55, 7
	s_add_i32 s0, s62, s89
	v_and_b32_e32 v49, 15, v48
	v_or_b32_e32 v125, s0, v49
	s_lshl_b32 s0, s57, 1
	s_waitcnt lgkmcnt(0)
	s_add_u32 s90, s10, s0
	v_and_b32_e32 v0, -16, v48
	s_addc_u32 s91, s11, 0
	v_mad_u64_u32 v[8:9], s[10:11], v125, s75, v[0:1]
	v_add_u32_e32 v4, 64, v8
	v_add_u32_e32 v9, 0x80, v8
	v_add_u32_e32 v12, 0xc0, v8
	global_load_dwordx4 v[0:3], v8, s[90:91]
	s_nop 0
	global_load_dwordx4 v[4:7], v4, s[90:91]
	s_nop 0
	global_load_dwordx4 v[8:11], v9, s[90:91]
	s_nop 0
	global_load_dwordx4 v[12:15], v12, s[90:91]
	s_lshl_b32 s1, s55, 1
	s_or_b32 s14, s1, 1
	s_waitcnt lgkmcnt(0)
	s_barrier
	s_mul_i32 s15, s14, 0x178000
	s_add_u32 s10, s90, s15
	s_addc_u32 s11, s91, 0
	v_lshl_add_u64 v[20:21], s[10:11], 0, v[104:105]
	global_load_dwordx4 v[16:19], v[20:21], off offset:1024
	v_add_co_u32_e32 v20, vcc, s86, v20
	v_add_u32_e32 v98, 0, v110
	s_nop 0
	v_addc_co_u32_e32 v21, vcc, 0, v21, vcc
	global_load_dwordx4 v[20:23], v[20:21], off offset:1024
	v_add_u32_e32 v99, 0, v111
	s_waitcnt vmcnt(0)
	ds_write_b128 v98, v[16:19]
	ds_write_b128 v99, v[20:23]
	s_waitcnt lgkmcnt(0)
	s_waitcnt lgkmcnt(0)
	s_barrier
	v_cndmask_b32_e64 v24, 0, 1, s[82:83]
	v_cmp_ne_u32_e64 s[10:11], 1, v24
	s_andn2_b64 vcc, exec, s[82:83]
	s_mul_i32 s55, s55, 0x2f0000
	s_cbranch_vccnz .LBB0_589
	s_add_u32 s12, s90, s55
	s_addc_u32 s13, s91, 0
	v_lshl_add_u64 v[16:17], s[12:13], 0, v[104:105]
	s_add_u32 s12, s90, s15
	v_add_co_u32_e32 v20, vcc, 0xbc000, v16
	s_addc_u32 s13, s91, 0
	s_nop 0
	v_addc_co_u32_e32 v21, vcc, 0, v17, vcc
	v_lshl_add_u64 v[24:25], s[12:13], 0, v[104:105]
	v_add_co_u32_e32 v28, vcc, 0xbc000, v24
	global_load_dwordx4 v[16:19], v[16:17], off offset:1024
	s_nop 0
	global_load_dwordx4 v[20:23], v[20:21], off offset:1024
	v_addc_co_u32_e32 v29, vcc, 0, v25, vcc
	global_load_dwordx4 v[24:27], v[24:25], off offset:2048
	s_nop 0
	global_load_dwordx4 v[28:31], v[28:29], off offset:2048
	s_waitcnt lgkmcnt(0)
	s_barrier

.LBB0_1977:
	s_and_b64 vcc, exec, s[6:7]
	s_cbranch_vccz .LBB0_1887
	s_and_b64 vcc, exec, s[74:75]
	s_cbranch_vccnz .Lprio_skip_1
	s_setprio 1
.Lprio_skip_1:
	s_sub_i32 s8, 63, s1
	s_load_dwordx2 s[4:5], s[52:53], 0x108
	s_load_dwordx2 s[84:85], s[52:53], 0x130
	v_mov_b32_e32 v48, v108
	s_lshl_b32 s62, s8, 7
	s_add_i32 s0, s62, s57
	v_and_b32_e32 v49, 15, v48
	v_or_b32_e32 v125, s0, v49
	v_readlane_b32 s0, v247, 38
	s_lshl_b32 s0, s0, 1
	s_waitcnt lgkmcnt(0)
	s_add_u32 s82, s4, s0
	v_and_b32_e32 v0, -16, v48
	s_addc_u32 s83, s5, 0
	v_mad_u64_u32 v[8:9], s[4:5], v125, s59, v[0:1]
	v_add_u32_e32 v4, 64, v8
	v_add_u32_e32 v9, 0x80, v8
	v_add_u32_e32 v12, 0xc0, v8
	global_load_dwordx4 v[0:3], v8, s[82:83]
	s_nop 0
	global_load_dwordx4 v[4:7], v4, s[82:83]
	s_nop 0
	global_load_dwordx4 v[8:11], v9, s[82:83]
	s_nop 0
	global_load_dwordx4 v[12:15], v12, s[82:83]
	s_lshl_b32 s4, s8, 1
	s_or_b32 s10, s4, 1
	s_waitcnt lgkmcnt(0)
	s_barrier
	s_mul_i32 s11, s10, 0x178000
	s_add_u32 s6, s82, s11
	s_addc_u32 s7, s83, 0
	v_lshl_add_u64 v[20:21], s[6:7], 0, v[104:105]
	global_load_dwordx4 v[16:19], v[20:21], off offset:1024
	v_add_co_u32_e32 v20, vcc, s51, v20
	v_add_u32_e32 v98, 0, v110
	s_nop 0
	v_addc_co_u32_e32 v21, vcc, 0, v21, vcc
	global_load_dwordx4 v[20:23], v[20:21], off offset:1024
	v_add_u32_e32 v99, 0, v111
	s_waitcnt vmcnt(0)
	ds_write_b128 v98, v[16:19]
	ds_write_b128 v99, v[20:23]
	s_waitcnt lgkmcnt(0)
	s_waitcnt lgkmcnt(0)
	s_barrier
	v_cndmask_b32_e64 v24, 0, 1, s[74:75]
	v_cmp_ne_u32_e64 s[6:7], 1, v24
	s_andn2_b64 vcc, exec, s[74:75]
	s_mul_i32 s5, s8, 0x2f0000
	s_cbranch_vccnz .LBB0_1980
	s_add_u32 s8, s82, s5
	s_addc_u32 s9, s83, 0
	v_lshl_add_u64 v[16:17], s[8:9], 0, v[104:105]
	s_add_u32 s8, s82, s11
	v_add_co_u32_e32 v20, vcc, 0xbc000, v16
	s_addc_u32 s9, s83, 0
	s_nop 0
	v_addc_co_u32_e32 v21, vcc, 0, v17, vcc
	v_lshl_add_u64 v[24:25], s[8:9], 0, v[104:105]
	v_add_co_u32_e32 v28, vcc, 0xbc000, v24
	global_load_dwordx4 v[16:19], v[16:17], off offset:1024
	s_nop 0
	global_load_dwordx4 v[20:23], v[20:21], off offset:1024
	v_addc_co_u32_e32 v29, vcc, 0, v25, vcc
	global_load_dwordx4 v[24:27], v[24:25], off offset:2048
	s_nop 0
	global_load_dwordx4 v[28:31], v[28:29], off offset:2048
	s_waitcnt lgkmcnt(0)
	s_barrier
